# speedup vs baseline: 1.0051x; 1.0051x over previous
.Lk1_nowarm9:
	buffer_load_dword v8, v1, s[8:11], s40 offen nt
	buffer_load_dword v9, v1, s[8:11], s41 offen nt
	buffer_load_dword v10, v1, s[8:11], s42 offen nt
	buffer_load_dword v11, v1, s[8:11], s43 offen nt
	buffer_load_dword v12, v1, s[8:11], s44 offen nt
	buffer_load_dword v13, v1, s[8:11], s45 offen nt
	buffer_load_dword v14, v1, s[8:11], s46 offen nt
	buffer_load_dword v15, v1, s[8:11], s47 offen nt
	buffer_load_dword v16, v1, s[8:11], s48 offen nt
	buffer_load_dword v17, v1, s[8:11], s49 offen nt
	buffer_load_dword v18, v1, s[8:11], s50 offen nt
	buffer_load_dword v19, v1, s[8:11], s51 offen nt
	buffer_load_dword v20, v1, s[8:11], s52 offen nt
	buffer_load_dword v21, v1, s[8:11], s53 offen nt
	buffer_load_dword v22, v1, s[8:11], s54 offen nt
	buffer_load_dword v23, v1, s[8:11], s55 offen nt
	s_add_u32 s8, s8, 0x4e200
	s_addc_u32 s9, s9, 0
	buffer_load_dword v24, v1, s[8:11], s40 offen nt
	buffer_load_dword v25, v1, s[8:11], s41 offen nt
	buffer_load_dword v26, v1, s[8:11], s42 offen nt
	buffer_load_dword v27, v1, s[8:11], s43 offen nt
	buffer_load_dword v28, v1, s[8:11], s44 offen nt
	buffer_load_dword v29, v1, s[8:11], s45 offen nt
	buffer_load_dword v30, v1, s[8:11], s46 offen nt
	buffer_load_dword v31, v1, s[8:11], s47 offen nt
	buffer_load_dword v32, v1, s[8:11], s48 offen nt
	buffer_load_dword v33, v1, s[8:11], s49 offen nt
	buffer_load_dword v34, v1, s[8:11], s50 offen nt
	buffer_load_dword v35, v1, s[8:11], s51 offen nt
	buffer_load_dword v36, v1, s[8:11], s52 offen nt
	buffer_load_dword v37, v1, s[8:11], s53 offen nt
	buffer_load_dword v38, v1, s[8:11], s54 offen nt
	buffer_load_dword v39, v1, s[8:11], s55 offen nt
	s_add_u32 s8, s8, 0x4e200
	s_addc_u32 s9, s9, 0
	buffer_load_dword v40, v1, s[8:11], s40 offen nt
	buffer_load_dword v41, v1, s[8:11], s41 offen nt
	buffer_load_dword v42, v1, s[8:11], s42 offen nt
	buffer_load_dword v43, v1, s[8:11], s43 offen nt
	buffer_load_dword v44, v1, s[8:11], s44 offen nt
	buffer_load_dword v45, v1, s[8:11], s45 offen nt
	buffer_load_dword v46, v1, s[8:11], s46 offen nt
	buffer_load_dword v47, v1, s[8:11], s47 offen nt
	buffer_load_dword v48, v1, s[8:11], s48 offen nt
	buffer_load_dword v49, v1, s[8:11], s49 offen nt
	buffer_load_dword v50, v1, s[8:11], s50 offen nt
	buffer_load_dword v51, v1, s[8:11], s51 offen nt
	buffer_load_dword v52, v1, s[8:11], s52 offen nt
	buffer_load_dword v53, v1, s[8:11], s53 offen nt
	buffer_load_dword v54, v1, s[8:11], s54 offen nt
	buffer_load_dword v55, v1, s[8:11], s55 offen nt
	s_add_u32 s8, s8, 0x4e200
	s_addc_u32 s9, s9, 0
	buffer_load_dword v56, v1, s[8:11], s40 offen nt
	buffer_load_dword v57, v1, s[8:11], s41 offen nt
	buffer_load_dword v58, v1, s[8:11], s42 offen nt
	buffer_load_dword v59, v1, s[8:11], s43 offen nt
	buffer_load_dword v60, v1, s[8:11], s44 offen nt
	buffer_load_dword v61, v1, s[8:11], s45 offen nt
	buffer_load_dword v62, v1, s[8:11], s46 offen nt
	buffer_load_dword v63, v1, s[8:11], s47 offen nt
	buffer_load_dword v64, v1, s[8:11], s48 offen nt
	buffer_load_dword v65, v1, s[8:11], s49 offen nt
	buffer_load_dword v66, v1, s[8:11], s50 offen nt
	v_mul_u32_u24_e32 v3, 0x147b, v2
	v_lshrrev_b32_e32 v3, 19, v3
	v_mul_u32_u24_e32 v98, 0x64, v3
	v_sub_u32_e32 v98, v2, v98
	v_add_u32_e32 v3, -1, v3
	v_add_u32_e32 v98, -1, v98
	s_movk_i32 s17, 0x62
	v_cmp_gt_u32_e64 s[36:37], 48, v3
	v_cmp_gt_u32_e64 s[38:39], s17, v98
	s_mul_i32 s17, s15, 0x1388
	v_add_lshl_u32 v98, v2, s17, 3
	s_and_b64 s[36:37], s[36:37], s[38:39]
	s_waitcnt vmcnt(55)
	buffer_load_dword v67, v1, s[8:11], s51 offen nt
	buffer_load_dword v68, v1, s[8:11], s52 offen nt
	buffer_load_dword v69, v1, s[8:11], s53 offen nt
	buffer_load_dword v70, v1, s[8:11], s54 offen nt
	buffer_load_dword v71, v1, s[8:11], s55 offen nt
	s_add_u32 s8, s8, 0x4e200
	s_addc_u32 s9, s9, 0
	buffer_load_dword v72, v1, s[8:11], s40 offen nt
	v_max3_f32 v76, v8, v9, v10
	v_max_f32_e32 v76, v76, v11
	v_sub_f32_e32 v8, v8, v76
	v_sub_f32_e32 v9, v9, v76
	v_sub_f32_e32 v10, v10, v76
	v_sub_f32_e32 v11, v11, v76
	v_or_b32_e32 v81, 0, v8
	v_or_b32_e32 v82, 1, v9
	v_min_u32_e32 v80, v81, v82
	v_or_b32_e32 v81, 2, v10
	v_or_b32_e32 v82, 3, v11
	v_min3_u32 v80, v80, v81, v82
	v_mul_f32_e32 v8, s14, v8
	v_mul_f32_e32 v9, s14, v9
	v_mul_f32_e32 v10, s14, v10
	v_mul_f32_e32 v11, s14, v11
	v_exp_f32_e32 v8, v8
	v_exp_f32_e32 v9, v9
	v_exp_f32_e32 v10, v10
	v_exp_f32_e32 v11, v11
	v_add_f32_e32 v78, v8, v10
	v_add_f32_e32 v79, v9, v11
	v_add_f32_e32 v78, v78, v79
	v_cvt_f64_f32_e32 v[86:87], v78
	v_mov_b32_e32 v75, v80
	v_mov_b32_e32 v73, v76
	s_waitcnt vmcnt(49)
	v_max3_f32 v76, v12, v13, v14
	v_max3_f32 v76, v76, v15, v16
	v_max3_f32 v76, v76, v17, v18
	v_max3_f32 v76, v76, v19, v20
	v_max3_f32 v76, v76, v21, v22
	v_max_f32_e32 v76, v76, v23
	v_max_f32_e32 v77, v73, v76
	v_cmp_gt_f32_e64 s[26:27], v76, v73
	v_sub_f32_e32 v83, v73, v77
	v_mul_f32_e32 v83, s14, v83
	v_exp_f32_e32 v83, v83
	v_sub_f32_e32 v12, v12, v77
	v_sub_f32_e32 v13, v13, v77
	v_sub_f32_e32 v14, v14, v77
	v_sub_f32_e32 v15, v15, v77
	v_sub_f32_e32 v16, v16, v77
	v_sub_f32_e32 v17, v17, v77
	v_sub_f32_e32 v18, v18, v77
	v_sub_f32_e32 v19, v19, v77
	v_sub_f32_e32 v20, v20, v77
	v_sub_f32_e32 v21, v21, v77
	v_sub_f32_e32 v22, v22, v77
	v_sub_f32_e32 v23, v23, v77
	v_cvt_f64_f32_e32 v[84:85], v83
	v_or_b32_e32 v81, 4, v12
	v_or_b32_e32 v82, 5, v13
	v_min_u32_e32 v80, v81, v82
	v_or_b32_e32 v81, 6, v14
	v_or_b32_e32 v82, 7, v15
	v_min3_u32 v80, v80, v81, v82
	v_or_b32_e32 v81, 8, v16
	v_or_b32_e32 v82, 9, v17
	v_min3_u32 v80, v80, v81, v82
	v_or_b32_e32 v81, 10, v18
	v_or_b32_e32 v82, 11, v19
	v_min3_u32 v80, v80, v81, v82
	v_or_b32_e32 v81, 12, v20
	v_or_b32_e32 v82, 13, v21
	v_min3_u32 v80, v80, v81, v82
	v_or_b32_e32 v81, 14, v22
	v_or_b32_e32 v82, 15, v23
	v_min3_u32 v80, v80, v81, v82
	v_mul_f64 v[86:87], v[86:87], v[84:85]
	v_mul_f32_e32 v12, s14, v12
	v_mul_f32_e32 v13, s14, v13
	v_mul_f32_e32 v14, s14, v14
	v_mul_f32_e32 v15, s14, v15
	v_mul_f32_e32 v16, s14, v16
	v_mul_f32_e32 v17, s14, v17
	v_mul_f32_e32 v18, s14, v18
	v_mul_f32_e32 v19, s14, v19
	v_mul_f32_e32 v20, s14, v20
	v_mul_f32_e32 v21, s14, v21
	v_mul_f32_e32 v22, s14, v22
	v_mul_f32_e32 v23, s14, v23
	v_exp_f32_e32 v12, v12
	v_exp_f32_e32 v13, v13
	v_exp_f32_e32 v14, v14
	v_exp_f32_e32 v15, v15
	v_exp_f32_e32 v16, v16
	v_exp_f32_e32 v17, v17
	v_exp_f32_e32 v18, v18
	v_exp_f32_e32 v19, v19
	v_exp_f32_e32 v20, v20
	v_exp_f32_e32 v21, v21
	v_exp_f32_e32 v22, v22
	v_exp_f32_e32 v23, v23
	v_add_f32_e32 v78, v12, v14
	v_add_f32_e32 v79, v13, v15
	v_add_f32_e32 v78, v78, v16
	v_add_f32_e32 v79, v79, v17
	v_add_f32_e32 v78, v78, v18
	v_add_f32_e32 v79, v79, v19
	v_add_f32_e32 v78, v78, v20
	v_add_f32_e32 v79, v79, v21
	v_add_f32_e32 v78, v78, v22
	v_add_f32_e32 v79, v79, v23
	v_add_f32_e32 v78, v78, v79
	v_cvt_f64_f32_e32 v[84:85], v78
	v_cndmask_b32_e64 v75, v75, v80, s[26:27]
	v_mov_b32_e32 v73, v77
	v_add_f64 v[86:87], v[86:87], v[84:85]
	s_waitcnt vmcnt(33)
	v_max3_f32 v76, v24, v25, v26
	v_max3_f32 v76, v76, v27, v28
	v_max3_f32 v76, v76, v29, v30
	v_max3_f32 v76, v76, v31, v32
	v_max3_f32 v76, v76, v33, v34
	v_max3_f32 v76, v76, v35, v36
	v_max3_f32 v76, v76, v37, v38
	v_max_f32_e32 v76, v76, v39
	v_max_f32_e32 v77, v73, v76
	v_cmp_gt_f32_e64 s[26:27], v76, v73
	v_sub_f32_e32 v83, v73, v77
	v_mul_f32_e32 v83, s14, v83
	v_exp_f32_e32 v83, v83
	v_sub_f32_e32 v24, v24, v77
	v_sub_f32_e32 v25, v25, v77
	v_sub_f32_e32 v26, v26, v77
	v_sub_f32_e32 v27, v27, v77
	v_sub_f32_e32 v28, v28, v77
	v_sub_f32_e32 v29, v29, v77
	v_sub_f32_e32 v30, v30, v77
	v_sub_f32_e32 v31, v31, v77
	v_sub_f32_e32 v32, v32, v77
	v_sub_f32_e32 v33, v33, v77
	v_sub_f32_e32 v34, v34, v77
	v_sub_f32_e32 v35, v35, v77
	v_sub_f32_e32 v36, v36, v77
	v_sub_f32_e32 v37, v37, v77
	v_sub_f32_e32 v38, v38, v77
	v_sub_f32_e32 v39, v39, v77
	v_cvt_f64_f32_e32 v[84:85], v83
	v_or_b32_e32 v81, 16, v24
	v_or_b32_e32 v82, 17, v25
	v_min_u32_e32 v80, v81, v82
	v_or_b32_e32 v81, 18, v26
	v_or_b32_e32 v82, 19, v27
	v_min3_u32 v80, v80, v81, v82
	v_or_b32_e32 v81, 20, v28
	v_or_b32_e32 v82, 21, v29
	v_min3_u32 v80, v80, v81, v82
	v_or_b32_e32 v81, 22, v30
	v_or_b32_e32 v82, 23, v31
	v_min3_u32 v80, v80, v81, v82
	v_or_b32_e32 v81, 24, v32
	v_or_b32_e32 v82, 25, v33
	v_min3_u32 v80, v80, v81, v82
	v_or_b32_e32 v81, 26, v34
	v_or_b32_e32 v82, 27, v35
	v_min3_u32 v80, v80, v81, v82
	v_or_b32_e32 v81, 28, v36
	v_or_b32_e32 v82, 29, v37
	v_min3_u32 v80, v80, v81, v82
	v_or_b32_e32 v81, 30, v38
	v_or_b32_e32 v82, 31, v39
	v_min3_u32 v80, v80, v81, v82
	v_mul_f64 v[86:87], v[86:87], v[84:85]
	v_mul_f32_e32 v24, s14, v24
	v_mul_f32_e32 v25, s14, v25
	v_mul_f32_e32 v26, s14, v26
	v_mul_f32_e32 v27, s14, v27
	v_mul_f32_e32 v28, s14, v28
	v_mul_f32_e32 v29, s14, v29
	v_mul_f32_e32 v30, s14, v30
	v_mul_f32_e32 v31, s14, v31
	v_mul_f32_e32 v32, s14, v32
	v_mul_f32_e32 v33, s14, v33
	v_mul_f32_e32 v34, s14, v34
	v_mul_f32_e32 v35, s14, v35
	v_mul_f32_e32 v36, s14, v36
	v_mul_f32_e32 v37, s14, v37
	v_mul_f32_e32 v38, s14, v38
	v_mul_f32_e32 v39, s14, v39
	v_exp_f32_e32 v24, v24
	v_exp_f32_e32 v25, v25
	v_exp_f32_e32 v26, v26
	v_exp_f32_e32 v27, v27
	v_exp_f32_e32 v28, v28
	v_exp_f32_e32 v29, v29
	v_exp_f32_e32 v30, v30
	v_exp_f32_e32 v31, v31
	v_exp_f32_e32 v32, v32
	v_exp_f32_e32 v33, v33
	v_exp_f32_e32 v34, v34
	v_exp_f32_e32 v35, v35
	v_exp_f32_e32 v36, v36
	v_exp_f32_e32 v37, v37
	v_exp_f32_e32 v38, v38
	v_exp_f32_e32 v39, v39
	v_add_f32_e32 v78, v24, v26
	v_add_f32_e32 v79, v25, v27
	v_add_f32_e32 v78, v78, v28
	v_add_f32_e32 v79, v79, v29
	v_add_f32_e32 v78, v78, v30
	v_add_f32_e32 v79, v79, v31
	v_add_f32_e32 v78, v78, v32
	v_add_f32_e32 v79, v79, v33
	v_add_f32_e32 v78, v78, v34
	v_add_f32_e32 v79, v79, v35
	v_add_f32_e32 v78, v78, v36
	v_add_f32_e32 v79, v79, v37
	v_add_f32_e32 v78, v78, v38
	v_add_f32_e32 v79, v79, v39
	v_add_f32_e32 v78, v78, v79
	v_cvt_f64_f32_e32 v[84:85], v78
	v_cndmask_b32_e64 v75, v75, v80, s[26:27]
	v_mov_b32_e32 v73, v77
	v_add_f64 v[86:87], v[86:87], v[84:85]
	s_waitcnt vmcnt(17)
	v_max3_f32 v76, v40, v41, v42
	v_max3_f32 v76, v76, v43, v44
	v_max3_f32 v76, v76, v45, v46
	v_max3_f32 v76, v76, v47, v48
	v_max3_f32 v76, v76, v49, v50
	v_max3_f32 v76, v76, v51, v52
	v_max3_f32 v76, v76, v53, v54
	v_max_f32_e32 v76, v76, v55
	v_max_f32_e32 v77, v73, v76
	v_cmp_gt_f32_e64 s[26:27], v76, v73
	v_sub_f32_e32 v83, v73, v77
	v_mul_f32_e32 v83, s14, v83
	v_exp_f32_e32 v83, v83
	v_sub_f32_e32 v40, v40, v77
	v_sub_f32_e32 v41, v41, v77
	v_sub_f32_e32 v42, v42, v77
	v_sub_f32_e32 v43, v43, v77
	v_sub_f32_e32 v44, v44, v77
	v_sub_f32_e32 v45, v45, v77
	v_sub_f32_e32 v46, v46, v77
	v_sub_f32_e32 v47, v47, v77
	v_sub_f32_e32 v48, v48, v77
	v_sub_f32_e32 v49, v49, v77
	v_sub_f32_e32 v50, v50, v77
	v_sub_f32_e32 v51, v51, v77
	v_sub_f32_e32 v52, v52, v77
	v_sub_f32_e32 v53, v53, v77
	v_sub_f32_e32 v54, v54, v77
	v_sub_f32_e32 v55, v55, v77
	v_cvt_f64_f32_e32 v[84:85], v83
	v_or_b32_e32 v81, 32, v40
	v_or_b32_e32 v82, 33, v41
	v_min_u32_e32 v80, v81, v82
	v_or_b32_e32 v81, 34, v42
	v_or_b32_e32 v82, 35, v43
	v_min3_u32 v80, v80, v81, v82
	v_or_b32_e32 v81, 36, v44
	v_or_b32_e32 v82, 37, v45
	v_min3_u32 v80, v80, v81, v82
	v_or_b32_e32 v81, 38, v46
	v_or_b32_e32 v82, 39, v47
	v_min3_u32 v80, v80, v81, v82
	v_or_b32_e32 v81, 40, v48
	v_or_b32_e32 v82, 41, v49
	v_min3_u32 v80, v80, v81, v82
	v_or_b32_e32 v81, 42, v50
	v_or_b32_e32 v82, 43, v51
	v_min3_u32 v80, v80, v81, v82
	v_or_b32_e32 v81, 44, v52
	v_or_b32_e32 v82, 45, v53
	v_min3_u32 v80, v80, v81, v82
	v_or_b32_e32 v81, 46, v54
	v_or_b32_e32 v82, 47, v55
	v_min3_u32 v80, v80, v81, v82
	v_mul_f64 v[86:87], v[86:87], v[84:85]
	v_mul_f32_e32 v40, s14, v40
	v_mul_f32_e32 v41, s14, v41
	v_mul_f32_e32 v42, s14, v42
	v_mul_f32_e32 v43, s14, v43
	v_mul_f32_e32 v44, s14, v44
	v_mul_f32_e32 v45, s14, v45
	v_mul_f32_e32 v46, s14, v46
	v_mul_f32_e32 v47, s14, v47
	v_mul_f32_e32 v48, s14, v48
	v_mul_f32_e32 v49, s14, v49
	v_mul_f32_e32 v50, s14, v50
	v_mul_f32_e32 v51, s14, v51
	v_mul_f32_e32 v52, s14, v52
	v_mul_f32_e32 v53, s14, v53
	v_mul_f32_e32 v54, s14, v54
	v_mul_f32_e32 v55, s14, v55
	v_exp_f32_e32 v40, v40
	v_exp_f32_e32 v41, v41
	v_exp_f32_e32 v42, v42
	v_exp_f32_e32 v43, v43
	v_exp_f32_e32 v44, v44
	v_exp_f32_e32 v45, v45
	v_exp_f32_e32 v46, v46
	v_exp_f32_e32 v47, v47
	v_exp_f32_e32 v48, v48
	v_exp_f32_e32 v49, v49
	v_exp_f32_e32 v50, v50
	v_exp_f32_e32 v51, v51
	v_exp_f32_e32 v52, v52
	v_exp_f32_e32 v53, v53
	v_exp_f32_e32 v54, v54
	v_exp_f32_e32 v55, v55
	v_add_f32_e32 v78, v40, v42
	v_add_f32_e32 v79, v41, v43
	v_add_f32_e32 v78, v78, v44
	v_add_f32_e32 v79, v79, v45
	v_add_f32_e32 v78, v78, v46
	v_add_f32_e32 v79, v79, v47
	v_add_f32_e32 v78, v78, v48
	v_add_f32_e32 v79, v79, v49
	v_add_f32_e32 v78, v78, v50
	v_add_f32_e32 v79, v79, v51
	v_add_f32_e32 v78, v78, v52
	v_add_f32_e32 v79, v79, v53
	v_add_f32_e32 v78, v78, v54
	v_add_f32_e32 v79, v79, v55
	v_add_f32_e32 v78, v78, v79
	v_cvt_f64_f32_e32 v[84:85], v78
	v_cndmask_b32_e64 v75, v75, v80, s[26:27]
	v_mov_b32_e32 v73, v77
	v_add_f64 v[86:87], v[86:87], v[84:85]
	s_waitcnt vmcnt(9)
	v_max3_f32 v76, v56, v57, v58
	v_max3_f32 v76, v76, v59, v60
	v_max3_f32 v76, v76, v61, v62
	v_max_f32_e32 v76, v76, v63
	v_max_f32_e32 v77, v73, v76
	v_cmp_gt_f32_e64 s[26:27], v76, v73
	v_sub_f32_e32 v83, v73, v77
	v_mul_f32_e32 v83, s14, v83
	v_exp_f32_e32 v83, v83
	v_sub_f32_e32 v56, v56, v77
	v_sub_f32_e32 v57, v57, v77
	v_sub_f32_e32 v58, v58, v77
	v_sub_f32_e32 v59, v59, v77
	v_sub_f32_e32 v60, v60, v77
	v_sub_f32_e32 v61, v61, v77
	v_sub_f32_e32 v62, v62, v77
	v_sub_f32_e32 v63, v63, v77
	v_cvt_f64_f32_e32 v[84:85], v83
	v_or_b32_e32 v81, 48, v56
	v_or_b32_e32 v82, 49, v57
	v_min_u32_e32 v80, v81, v82
	v_or_b32_e32 v81, 50, v58
	v_or_b32_e32 v82, 51, v59
	v_min3_u32 v80, v80, v81, v82
	v_or_b32_e32 v81, 52, v60
	v_or_b32_e32 v82, 53, v61
	v_min3_u32 v80, v80, v81, v82
	v_or_b32_e32 v81, 54, v62
	v_or_b32_e32 v82, 55, v63
	v_min3_u32 v80, v80, v81, v82
	v_mul_f64 v[86:87], v[86:87], v[84:85]
	v_mul_f32_e32 v56, s14, v56
	v_mul_f32_e32 v57, s14, v57
	v_mul_f32_e32 v58, s14, v58
	v_mul_f32_e32 v59, s14, v59
	v_mul_f32_e32 v60, s14, v60
	v_mul_f32_e32 v61, s14, v61
	v_mul_f32_e32 v62, s14, v62
	v_mul_f32_e32 v63, s14, v63
	v_exp_f32_e32 v56, v56
	v_exp_f32_e32 v57, v57
	v_exp_f32_e32 v58, v58
	v_exp_f32_e32 v59, v59
	v_exp_f32_e32 v60, v60
	v_exp_f32_e32 v61, v61
	v_exp_f32_e32 v62, v62
	v_exp_f32_e32 v63, v63
	v_add_f32_e32 v78, v56, v58
	v_add_f32_e32 v79, v57, v59
	v_add_f32_e32 v78, v78, v60
	v_add_f32_e32 v79, v79, v61
	v_add_f32_e32 v78, v78, v62
	v_add_f32_e32 v79, v79, v63
	v_add_f32_e32 v78, v78, v79
	v_cvt_f64_f32_e32 v[84:85], v78
	v_cndmask_b32_e64 v75, v75, v80, s[26:27]
	v_mov_b32_e32 v73, v77
	v_add_f64 v[86:87], v[86:87], v[84:85]
	s_waitcnt vmcnt(5)
	v_max3_f32 v76, v64, v65, v66
	v_max_f32_e32 v76, v76, v67
	v_max_f32_e32 v77, v73, v76
	v_cmp_gt_f32_e64 s[26:27], v76, v73
	v_sub_f32_e32 v83, v73, v77
	v_mul_f32_e32 v83, s14, v83
	v_exp_f32_e32 v83, v83
	v_sub_f32_e32 v64, v64, v77
	v_sub_f32_e32 v65, v65, v77
	v_sub_f32_e32 v66, v66, v77
	v_sub_f32_e32 v67, v67, v77
	v_cvt_f64_f32_e32 v[84:85], v83
	v_or_b32_e32 v81, 56, v64
	v_or_b32_e32 v82, 57, v65
	v_min_u32_e32 v80, v81, v82
	v_or_b32_e32 v81, 58, v66
	v_or_b32_e32 v82, 59, v67
	v_min3_u32 v80, v80, v81, v82
	v_mul_f64 v[86:87], v[86:87], v[84:85]
	v_mul_f32_e32 v64, s14, v64
	v_mul_f32_e32 v65, s14, v65
	v_mul_f32_e32 v66, s14, v66
	v_mul_f32_e32 v67, s14, v67
	v_exp_f32_e32 v64, v64
	v_exp_f32_e32 v65, v65
	v_exp_f32_e32 v66, v66
	v_exp_f32_e32 v67, v67
	v_add_f32_e32 v78, v64, v66
	v_add_f32_e32 v79, v65, v67
	v_add_f32_e32 v78, v78, v79
	v_cvt_f64_f32_e32 v[84:85], v78
	v_cndmask_b32_e64 v75, v75, v80, s[26:27]
	v_mov_b32_e32 v73, v77
	v_add_f64 v[86:87], v[86:87], v[84:85]
	s_waitcnt vmcnt(4)
	v_max_f32_e32 v77, v73, v68
	v_cmp_gt_f32_e64 s[26:27], v68, v73
	v_sub_f32_e32 v83, v73, v77
	v_sub_f32_e32 v68, v68, v77
	v_mul_f32_e32 v83, s14, v83
	v_mul_f32_e32 v68, s14, v68
	v_exp_f32_e32 v83, v83
	v_exp_f32_e32 v68, v68
	v_cndmask_b32_e64 v75, v75, 60, s[26:27]
	v_cvt_f64_f32_e32 v[84:85], v83
	v_cvt_f64_f32_e32 v[90:91], v68
	v_mul_f64 v[86:87], v[86:87], v[84:85]
	v_mov_b32_e32 v73, v77
	v_add_f64 v[86:87], v[86:87], v[90:91]
	s_waitcnt vmcnt(3)
	v_max_f32_e32 v77, v73, v69
	v_cmp_gt_f32_e64 s[26:27], v69, v73
	v_sub_f32_e32 v83, v73, v77
	v_sub_f32_e32 v69, v69, v77
	v_mul_f32_e32 v83, s14, v83
	v_mul_f32_e32 v69, s14, v69
	v_exp_f32_e32 v83, v83
	v_exp_f32_e32 v69, v69
	v_cndmask_b32_e64 v75, v75, 61, s[26:27]
	v_cvt_f64_f32_e32 v[84:85], v83
	v_cvt_f64_f32_e32 v[90:91], v69
	v_mul_f64 v[86:87], v[86:87], v[84:85]
	v_mov_b32_e32 v73, v77
	v_add_f64 v[86:87], v[86:87], v[90:91]
	s_waitcnt vmcnt(2)
	v_max_f32_e32 v77, v73, v70
	v_cmp_gt_f32_e64 s[26:27], v70, v73
	v_sub_f32_e32 v83, v73, v77
	v_sub_f32_e32 v70, v70, v77
	v_mul_f32_e32 v83, s14, v83
	v_mul_f32_e32 v70, s14, v70
	v_exp_f32_e32 v83, v83
	v_exp_f32_e32 v70, v70
	v_cndmask_b32_e64 v75, v75, 62, s[26:27]
	v_cvt_f64_f32_e32 v[84:85], v83
	v_cvt_f64_f32_e32 v[90:91], v70
	v_mul_f64 v[86:87], v[86:87], v[84:85]
	v_mov_b32_e32 v73, v77
	v_add_f64 v[86:87], v[86:87], v[90:91]
	s_waitcnt vmcnt(1)
	v_max_f32_e32 v77, v73, v71
	v_cmp_gt_f32_e64 s[26:27], v71, v73
	v_sub_f32_e32 v83, v73, v77
	v_sub_f32_e32 v71, v71, v77
	v_mul_f32_e32 v83, s14, v83
	v_mul_f32_e32 v71, s14, v71
	v_exp_f32_e32 v83, v83
	v_exp_f32_e32 v71, v71
	v_cndmask_b32_e64 v75, v75, 63, s[26:27]
	v_cvt_f64_f32_e32 v[84:85], v83
	v_cvt_f64_f32_e32 v[90:91], v71
	v_mul_f64 v[86:87], v[86:87], v[84:85]
	v_mov_b32_e32 v73, v77
	v_add_f64 v[86:87], v[86:87], v[90:91]
	s_waitcnt vmcnt(0)
	v_max_f32_e32 v77, v73, v72
	v_cmp_gt_f32_e64 s[26:27], v72, v73
	v_sub_f32_e32 v83, v73, v77
	v_sub_f32_e32 v72, v72, v77
	v_mul_f32_e32 v83, s14, v83
	v_mul_f32_e32 v72, s14, v72
	v_exp_f32_e32 v83, v83
	v_exp_f32_e32 v72, v72
	v_cndmask_b32_e64 v75, v75, 64, s[26:27]
	v_cvt_f64_f32_e32 v[84:85], v83
	v_cvt_f64_f32_e32 v[90:91], v72
	v_mul_f64 v[86:87], v[86:87], v[84:85]
	v_add_f64 v[86:87], v[86:87], v[90:91]
	v_rcp_f64_e32 v[88:89], v[86:87]
	v_cmp_gt_u32_e32 vcc, 64, v75
	s_and_b64 vcc, vcc, s[36:37]
	v_fma_f64 v[90:91], -v[86:87], v[88:89], 1.0
	v_fma_f64 v[88:89], v[90:91], v[88:89], v[88:89]
	v_cvt_f32_f64_e32 v3, v[88:89]
	v_cndmask_b32_e32 v74, 0, v3, vcc
	global_store_dwordx2 v98, v[74:75], s[6:7]
